# 64 converter workgroups instead of 56 (compute group 192: the input projection is exactly 11 full rounds) on top of the converter walk wait fix
# speedup vs baseline: 1.0215x; 1.0215x over previous
; __global__ void __launch_bounds__(512, 2) mega_fwd(Args args) {
;     ...
;     const int NC = ovl ? CONV_NC : 0, Gc = G - NC, cx = bx - NC; const bool is_conv = bx < NC;
;     XcdBarrier bar; bar.bar = ctl + CW_BAR; bar.x = 0; bar.st = nullptr; bar.G = (unsigned)G;
;     ...
;     XcdBarrier barc = bar;
;     if (ovl && !is_conv) barc = xcd_barrier_post(ctl + CW_BAR2, MISC + 10, (unsigned)Gc);
.LBB0_12:
	s_or_b64 exec, exec, s[4:5]
	s_and_b64 s[4:5], s[34:35], exec
	s_cselect_b32 s87, 64, 0
	s_sub_i32 s85, s82, s87
	s_cmp_lt_i32 s2, s87
	s_cselect_b64 s[4:5], -1, 0
	s_cmp_ge_i32 s2, s87
	s_cselect_b64 s[6:7], -1, 0
	s_and_b64 s[6:7], s[34:35], s[6:7]
	s_andn2_b64 vcc, exec, s[6:7]
	s_cbranch_vccnz .LBB0_17
	s_add_u32 s36, s18, 0x8000
	s_getreg_b32 s3, hwreg(HW_REG_XCC_ID, 0, 4)
	s_addc_u32 s37, s19, 0
	s_and_b32 s77, s3, 15
	s_and_saveexec_b64 s[6:7], s[14:15]
	s_cbranch_execz .LBB0_16
	s_mov_b64 s[8:9], exec
	v_mbcnt_lo_u32_b32 v2, s8, 0
	v_mbcnt_hi_u32_b32 v2, s9, v2
	v_cmp_eq_u32_e32 vcc, 0, v2
	s_and_b64 s[10:11], exec, vcc
	s_mov_b64 exec, s[10:11]
	s_cbranch_execz .LBB0_16
	s_lshl_b32 s3, s77, 8
	s_bcnt1_i32_b64 s8, s[8:9]
	v_mov_b32_e32 v2, s3
	v_mov_b32_e32 v3, s8
	global_atomic_add v2, v3, s[36:37] offset:1024
